# speedup vs baseline: 1.0113x; 1.0113x over previous
_Z8gemm_f16ILi256ELi160ELi4ELi2ELi2ELi1ELi1EEvPKDF16_S1_Pviiii:
	s_load_dwordx4 s[12:15], s[0:1], 0x0
	s_load_dwordx2 s[0:1], s[0:1], 0x10
	s_and_b32 s3, s2, 3
	s_mul_i32 s3, s3, 30
	s_lshr_b32 s6, s2, 3
	s_add_i32 s3, s3, s6
	s_and_b32 s6, s2, 4
	s_and_b32 s7, s3, 3
	s_or_b32 s6, s6, s7
	s_lshl_b32 s10, s6, 8
	s_lshr_b32 s2, s3, 2
	s_mulk_i32 s2, 0xa0
	s_movk_i32 s5, 0x12c0
	v_lshrrev_b32_e32 v95, 3, v0
	v_and_b32_e32 v99, 7, v0
	v_bfe_u32 v91, v0, 4, 3
	v_xor_b32_e32 v99, v99, v91
	v_lshlrev_b32_e32 v99, 4, v99
	v_add_u32_e32 v91, s10, v95
	v_lshl_add_u32 v82, v91, 11, v99
	v_add_u32_e32 v83, 0x20000, v82
	v_add_u32_e32 v84, 0x40000, v82
	v_add_u32_e32 v85, 0x60000, v82
	v_add_u32_e32 v91, s2, v95
	v_lshl_add_u32 v86, v91, 11, v99
	v_add_u32_e32 v87, 0x20000, v86
	v_add_u32_e32 v88, 0x40000, v86
	v_lshlrev_b32_e32 v95, 4, v0
	s_nop 0
	v_readfirstlane_b32 s20, v95
	s_mov_b32 s29, 0xa000
	s_cmp_lt_u32 s20, 0x1000
	s_cselect_b32 s29, 0xc000, s29
	s_cbranch_scc1 .Lg1_w03
	v_mov_b32_e32 v88, v87
